# k_bin: batched bucket-offset reads for the LDS scatter, unrolled copy-out (all LDS reads issued before the stores)
# speedup vs baseline: 1.0186x; 1.0031x over previous
.LBB0_15:
	s_or_b64 exec, exec, s[6:7]
	s_waitcnt lgkmcnt(0)
	s_barrier
	v_lshlrev_b32_e32 v27, 2, v27
	v_lshlrev_b32_e32 v25, 2, v25
	v_lshlrev_b32_e32 v23, 2, v23
	v_lshlrev_b32_e32 v22, 2, v22
	ds_read_b32 v62, v55 offset:13536
	ds_read_b32 v63, v53 offset:13536
	ds_read_b32 v64, v49 offset:13536
	ds_read_b32 v65, v45 offset:13536
	ds_read_b32 v66, v42 offset:13536
	ds_read_b32 v67, v39 offset:13536
	ds_read_b32 v68, v37 offset:13536
	ds_read_b32 v69, v35 offset:13536
	ds_read_b32 v70, v32 offset:13536
	ds_read_b32 v71, v27 offset:13536
	ds_read_b32 v72, v25 offset:13536
	ds_read_b32 v73, v23 offset:13536
	ds_read_b32 v74, v22 offset:13536
	s_load_dwordx2 s[6:7], s[0:1], 0x10
	s_mov_b32 s3, 0x6050400
	v_perm_b32 v50, v50, v52, s3
	v_perm_b32 v46, v46, v47, s3
	v_perm_b32 v43, v43, v33, s3
	v_perm_b32 v40, v40, v30, s3
	v_perm_b32 v28, v28, v29, s3
	v_perm_b32 v20, v20, v21, s3
	v_perm_b32 v16, v16, v17, s3
	v_perm_b32 v15, v15, v14, s3
	v_perm_b32 v12, v12, v13, s3
	v_perm_b32 v10, v10, v11, s3
	v_perm_b32 v8, v8, v9, s3
	v_perm_b32 v6, v6, v7, s3
	v_perm_b32 v1, v1, v3, s3
	s_waitcnt lgkmcnt(0)
	v_cmp_lt_i32_e32 vcc, -1, v54
	s_and_saveexec_b64 s[8:9], vcc
	v_add_lshl_u32 v62, v62, v54, 2
	ds_write_b32 v62, v50
	s_mov_b64 exec, s[8:9]
	v_cmp_lt_i32_e32 vcc, -1, v51
	s_and_saveexec_b64 s[8:9], vcc
	v_add_lshl_u32 v63, v63, v51, 2
	ds_write_b32 v63, v46
	s_mov_b64 exec, s[8:9]
	v_cmp_lt_i32_e32 vcc, -1, v48
	s_and_saveexec_b64 s[8:9], vcc
	v_add_lshl_u32 v64, v64, v48, 2
	ds_write_b32 v64, v43
	s_mov_b64 exec, s[8:9]
	v_cmp_lt_i32_e32 vcc, -1, v44
	s_and_saveexec_b64 s[8:9], vcc
	v_add_lshl_u32 v65, v65, v44, 2
	ds_write_b32 v65, v40
	s_mov_b64 exec, s[8:9]
	v_cmp_lt_i32_e32 vcc, -1, v41
	s_and_saveexec_b64 s[8:9], vcc
	v_add_lshl_u32 v66, v66, v41, 2
	ds_write_b32 v66, v28
	s_mov_b64 exec, s[8:9]
	v_cmp_lt_i32_e32 vcc, -1, v38
	s_and_saveexec_b64 s[8:9], vcc
	v_add_lshl_u32 v67, v67, v38, 2
	ds_write_b32 v67, v20
	s_mov_b64 exec, s[8:9]
	v_cmp_lt_i32_e32 vcc, -1, v36
	s_and_saveexec_b64 s[8:9], vcc
	v_add_lshl_u32 v68, v68, v36, 2
	ds_write_b32 v68, v16
	s_mov_b64 exec, s[8:9]
	v_cmp_lt_i32_e32 vcc, -1, v34
	s_and_saveexec_b64 s[8:9], vcc
	v_add_lshl_u32 v69, v69, v34, 2
	ds_write_b32 v69, v15
	s_mov_b64 exec, s[8:9]
	v_cmp_lt_i32_e32 vcc, -1, v31
	s_and_saveexec_b64 s[8:9], vcc
	v_add_lshl_u32 v70, v70, v31, 2
	ds_write_b32 v70, v12
	s_mov_b64 exec, s[8:9]
	v_cmp_lt_i32_e32 vcc, -1, v26
	s_and_saveexec_b64 s[8:9], vcc
	v_add_lshl_u32 v71, v71, v26, 2
	ds_write_b32 v71, v10
	s_mov_b64 exec, s[8:9]
	v_cmp_lt_i32_e32 vcc, -1, v19
	s_and_saveexec_b64 s[8:9], vcc
	v_add_lshl_u32 v72, v72, v19, 2
	ds_write_b32 v72, v8
	s_mov_b64 exec, s[8:9]
	v_cmp_lt_i32_e32 vcc, -1, v24
	s_and_saveexec_b64 s[8:9], vcc
	v_add_lshl_u32 v73, v73, v24, 2
	ds_write_b32 v73, v6
	s_mov_b64 exec, s[8:9]
	v_cmp_lt_i32_e32 vcc, -1, v18
	s_and_saveexec_b64 s[8:9], vcc
	v_add_lshl_u32 v74, v74, v18, 2
	ds_write_b32 v74, v1
	s_mov_b64 exec, s[8:9]
	v_add_u32_e32 v4, s4, v0
	v_mov_b32_e32 v5, 0
	v_lshl_add_u64 v[4:5], v[4:5], 2, s[6:7]
	s_mov_b64 s[6:7], 0x1000
	s_waitcnt lgkmcnt(0)
	s_barrier
	ds_read_b32 v62, v2
	ds_read_b32 v63, v2 offset:1024
	ds_read_b32 v64, v2 offset:2048
	ds_read_b32 v65, v2 offset:3072
	ds_read_b32 v66, v2 offset:4096
	ds_read_b32 v67, v2 offset:5120
	ds_read_b32 v68, v2 offset:6144
	ds_read_b32 v69, v2 offset:7168
	ds_read_b32 v70, v2 offset:8192
	ds_read_b32 v71, v2 offset:9216
	ds_read_b32 v72, v2 offset:10240
	ds_read_b32 v73, v2 offset:11264
	ds_read_b32 v74, v2 offset:12288
	s_waitcnt lgkmcnt(0)
	global_store_dword v[4:5], v62, off
	global_store_dword v[4:5], v63, off offset:1024
	global_store_dword v[4:5], v64, off offset:2048
	global_store_dword v[4:5], v65, off offset:3072
	v_lshl_add_u64 v[4:5], v[4:5], 0, s[6:7]
	global_store_dword v[4:5], v66, off
	global_store_dword v[4:5], v67, off offset:1024
	global_store_dword v[4:5], v68, off offset:2048
	global_store_dword v[4:5], v69, off offset:3072
	v_lshl_add_u64 v[4:5], v[4:5], 0, s[6:7]
	global_store_dword v[4:5], v70, off
	global_store_dword v[4:5], v71, off offset:1024
	global_store_dword v[4:5], v72, off offset:2048
	global_store_dword v[4:5], v73, off offset:3072
	v_lshl_add_u64 v[4:5], v[4:5], 0, s[6:7]
	v_cmp_gt_u32_e32 vcc, 53, v0
	s_and_b64 exec, exec, vcc
	global_store_dword v[4:5], v74, off
	s_branch .LBB0_2

.LBB0_36:
	s_or_b64 exec, exec, s[4:5]
	v_lshl_or_b32 v0, s2, 8, v0
	v_add_u32_e32 v4, 0xffff0000, v0
	v_ashrrev_i32_e32 v5, 5, v4
	v_subrev_u32_e32 v5, 32, v5
	v_mov_b32_e32 v3, 0
	v_and_b32_e32 v16, -8, v5
	s_waitcnt lgkmcnt(0)
	v_lshl_add_u64 v[0:1], s[12:13], 0, v[2:3]
	s_movk_i32 s12, 0x598
	v_mov_b32_e32 v18, 0x597
	v_cmp_gt_u32_e32 vcc, s12, v16
	v_or_b32_e32 v6, 1, v16
	v_or_b32_e32 v8, 2, v16
	v_cndmask_b32_e32 v2, v18, v16, vcc
	v_or_b32_e32 v10, 3, v16
	v_or_b32_e32 v12, 4, v16
	v_or_b32_e32 v14, 5, v16
	v_or_b32_e32 v16, 6, v16
	v_or_b32_e32 v5, 7, v5
	v_cmp_gt_u32_e64 s[0:1], s12, v6
	v_cmp_gt_u32_e64 s[2:3], s12, v8
	v_cmp_gt_u32_e64 s[4:5], s12, v10
	v_cmp_gt_u32_e64 s[6:7], s12, v12
	v_cmp_gt_u32_e64 s[8:9], s12, v14
	v_cmp_gt_u32_e64 s[10:11], s12, v16
	v_cmp_gt_u32_e64 s[12:13], s12, v5
	v_ashrrev_i32_e32 v3, 31, v2
	v_cndmask_b32_e64 v6, v18, v6, s[0:1]
	v_cndmask_b32_e64 v8, v18, v8, s[2:3]
	v_cndmask_b32_e64 v10, v18, v10, s[4:5]
	v_cndmask_b32_e64 v12, v18, v12, s[6:7]
	v_cndmask_b32_e64 v14, v18, v14, s[8:9]
	v_cndmask_b32_e64 v16, v18, v16, s[10:11]
	v_cndmask_b32_e64 v18, v18, v5, s[12:13]
	v_lshlrev_b64 v[2:3], 10, v[2:3]
	v_ashrrev_i32_e32 v7, 31, v6
	v_ashrrev_i32_e32 v9, 31, v8
	v_ashrrev_i32_e32 v11, 31, v10
	v_ashrrev_i32_e32 v13, 31, v12
	v_ashrrev_i32_e32 v15, 31, v14
	v_ashrrev_i32_e32 v17, 31, v16
	v_ashrrev_i32_e32 v19, 31, v18
	v_lshl_add_u64 v[2:3], v[0:1], 0, v[2:3]
	v_lshlrev_b64 v[6:7], 10, v[6:7]
	v_lshlrev_b64 v[8:9], 10, v[8:9]
	v_lshlrev_b64 v[10:11], 10, v[10:11]
	v_lshlrev_b64 v[12:13], 10, v[12:13]
	v_lshlrev_b64 v[14:15], 10, v[14:15]
	v_lshlrev_b64 v[16:17], 10, v[16:17]
	v_lshlrev_b64 v[18:19], 10, v[18:19]
	v_lshl_add_u64 v[6:7], v[0:1], 0, v[6:7]
	v_lshl_add_u64 v[8:9], v[0:1], 0, v[8:9]
	v_lshl_add_u64 v[10:11], v[0:1], 0, v[10:11]
	v_lshl_add_u64 v[12:13], v[0:1], 0, v[12:13]
	v_lshl_add_u64 v[14:15], v[0:1], 0, v[14:15]
	v_lshl_add_u64 v[16:17], v[0:1], 0, v[16:17]
	v_lshl_add_u64 v[0:1], v[0:1], 0, v[18:19]
	global_load_dword v18, v[2:3], off
	global_load_dword v19, v[6:7], off
	global_load_dword v20, v[8:9], off
	global_load_dword v21, v[10:11], off
	global_load_dword v22, v[12:13], off
	global_load_dword v23, v[14:15], off
	global_load_dword v24, v[16:17], off
	global_load_dword v25, v[0:1], off
	v_ashrrev_i32_e32 v5, 31, v4
	v_lshl_add_u64 v[4:5], v[4:5], 4, s[14:15]
	s_waitcnt vmcnt(7)
	v_cvt_f16_f32_e32 v0, v18
	s_waitcnt vmcnt(6)
	v_cvt_f16_f32_e32 v1, v19
	s_waitcnt vmcnt(5)
	v_cvt_f16_f32_e32 v2, v20
	s_waitcnt vmcnt(4)
	v_cvt_f16_f32_e32 v3, v21
	s_waitcnt vmcnt(3)
	v_cvt_f16_f32_e32 v6, v22
	s_waitcnt vmcnt(2)
	v_cvt_f16_f32_e32 v7, v23
	s_waitcnt vmcnt(1)
	v_cvt_f16_f32_e32 v8, v24
	s_waitcnt vmcnt(0)
	v_cvt_f16_f32_e32 v9, v25
	v_cndmask_b32_e32 v0, 0, v0, vcc
	v_cndmask_b32_e64 v10, 0, v1, s[0:1]
	v_cndmask_b32_e64 v1, 0, v2, s[2:3]
	v_cndmask_b32_e64 v11, 0, v3, s[4:5]
	v_cndmask_b32_e64 v2, 0, v6, s[6:7]
	v_cndmask_b32_e64 v6, 0, v7, s[8:9]
	v_cndmask_b32_e64 v3, 0, v8, s[10:11]
	v_cndmask_b32_e64 v7, 0, v9, s[12:13]
	v_pack_b32_f16 v3, v3, v7
	v_pack_b32_f16 v2, v2, v6
	v_pack_b32_f16 v1, v1, v11
	v_pack_b32_f16 v0, v0, v10
	global_store_dwordx4 v[4:5], v[0:3], off
	s_endpgm
	.section	.rodata,"a",@progbits
	.p2align	6, 0x0
	.amdhsa_kernel _Z5k_binPKiPiPjPKfPDv8_DF16_PDF16_
		.amdhsa_group_segment_fixed_size 14576
		.amdhsa_private_segment_fixed_size 0
		.amdhsa_kernarg_size 48
		.amdhsa_user_sgpr_count 2
		.amdhsa_user_sgpr_dispatch_ptr 0
		.amdhsa_user_sgpr_queue_ptr 0
		.amdhsa_user_sgpr_kernarg_segment_ptr 1
		.amdhsa_user_sgpr_dispatch_id 0
		.amdhsa_user_sgpr_kernarg_preload_length 0
		.amdhsa_user_sgpr_kernarg_preload_offset 0
		.amdhsa_user_sgpr_private_segment_size 0
		.amdhsa_uses_dynamic_stack 0
		.amdhsa_enable_private_segment 0
		.amdhsa_system_sgpr_workgroup_id_x 1
		.amdhsa_system_sgpr_workgroup_id_y 0
		.amdhsa_system_sgpr_workgroup_id_z 0
		.amdhsa_system_sgpr_workgroup_info 0
		.amdhsa_system_vgpr_workitem_id 0
		.amdhsa_next_free_vgpr 75
		.amdhsa_next_free_sgpr 16
		.amdhsa_accum_offset 76
		.amdhsa_reserve_vcc 1
		.amdhsa_float_round_mode_32 0
		.amdhsa_float_round_mode_16_64 0
		.amdhsa_float_denorm_mode_32 3
		.amdhsa_float_denorm_mode_16_64 3
		.amdhsa_dx10_clamp 1
		.amdhsa_ieee_mode 1
		.amdhsa_fp16_overflow 0
		.amdhsa_tg_split 0
		.amdhsa_exception_fp_ieee_invalid_op 0
		.amdhsa_exception_fp_denorm_src 0
		.amdhsa_exception_fp_ieee_div_zero 0
		.amdhsa_exception_fp_ieee_overflow 0
		.amdhsa_exception_fp_ieee_underflow 0
		.amdhsa_exception_fp_ieee_inexact 0
		.amdhsa_exception_int_div_zero 0
	.end_amdhsa_kernel

amdhsa.kernels:
  - .agpr_count:     0
    .args:
      - .actual_access:  read_only
        .address_space:  global
        .offset:         0
        .size:           8
        .value_kind:     global_buffer
      - .actual_access:  write_only
        .address_space:  global
        .offset:         8
        .size:           8
        .value_kind:     global_buffer
      - .actual_access:  write_only
        .address_space:  global
        .offset:         16
        .size:           8
        .value_kind:     global_buffer
      - .actual_access:  read_only
        .address_space:  global
        .offset:         24
        .size:           8
        .value_kind:     global_buffer
      - .actual_access:  write_only
        .address_space:  global
        .offset:         32
        .size:           8
        .value_kind:     global_buffer
      - .actual_access:  write_only
        .address_space:  global
        .offset:         40
        .size:           8
        .value_kind:     global_buffer
    .group_segment_fixed_size: 14576
    .kernarg_segment_align: 8
    .kernarg_segment_size: 48
    .language:       OpenCL C
    .language_version:
      - 2
      - 0
    .max_flat_workgroup_size: 256
    .name:           _Z5k_binPKiPiPjPKfPDv8_DF16_PDF16_
    .private_segment_fixed_size: 0
    .sgpr_count:     22
    .sgpr_spill_count: 0
    .symbol:         _Z5k_binPKiPiPjPKfPDv8_DF16_PDF16_.kd
    .uniform_work_group_size: 1
    .uses_dynamic_stack: false
    .vgpr_count:     75
    .vgpr_spill_count: 0
    .wavefront_size: 64
  - .agpr_count:     0
    .args:
      - .actual_access:  read_only
        .address_space:  global
        .offset:         0
        .size:           8
        .value_kind:     global_buffer
      - .actual_access:  read_only
        .address_space:  global
        .offset:         8
        .size:           8
        .value_kind:     global_buffer
      - .actual_access:  write_only
        .address_space:  global
        .offset:         16
        .size:           8
        .value_kind:     global_buffer
      - .actual_access:  write_only
        .address_space:  global
        .offset:         24
        .size:           8
        .value_kind:     global_buffer
      - .actual_access:  write_only
        .address_space:  global
        .offset:         32
        .size:           8
        .value_kind:     global_buffer
      - .actual_access:  write_only
        .address_space:  global
        .offset:         40
        .size:           8
        .value_kind:     global_buffer
    .group_segment_fixed_size: 18452
    .kernarg_segment_align: 8
    .kernarg_segment_size: 48
    .language:       OpenCL C
    .language_version:
      - 2
      - 0
    .max_flat_workgroup_size: 256
    .name:           _Z5k_csrPKiPKjP15HIP_vector_typeIiLj2EEPfPtS6_
    .private_segment_fixed_size: 0
    .sgpr_count:     94
    .sgpr_spill_count: 0
    .symbol:         _Z5k_csrPKiPKjP15HIP_vector_typeIiLj2EEPfPtS6_.kd
    .uniform_work_group_size: 1
    .uses_dynamic_stack: false
    .vgpr_count:     65
    .vgpr_spill_count: 0
    .wavefront_size: 64
  - .agpr_count:     0
    .args:
      - .actual_access:  read_only
        .address_space:  global
        .offset:         0
        .size:           8
        .value_kind:     global_buffer
      - .actual_access:  read_only
        .address_space:  global
        .offset:         8
        .size:           8
        .value_kind:     global_buffer
      - .actual_access:  read_only
        .address_space:  global
        .offset:         16
        .size:           8
        .value_kind:     global_buffer
      - .actual_access:  read_only
        .address_space:  global
        .offset:         24
        .size:           8
        .value_kind:     global_buffer
      - .actual_access:  write_only
        .address_space:  global
        .offset:         32
        .size:           8
        .value_kind:     global_buffer
    .group_segment_fixed_size: 129152
    .kernarg_segment_align: 8
    .kernarg_segment_size: 40
    .language:       OpenCL C
    .language_version:
      - 2
      - 0
    .max_flat_workgroup_size: 512
    .name:           _Z6k_gemmPKfPKDv8_DF16_S0_S0_PDF16_
    .private_segment_fixed_size: 0
    .sgpr_count:     22
    .sgpr_spill_count: 0
    .symbol:         _Z6k_gemmPKfPKDv8_DF16_S0_S0_PDF16_.kd
    .uniform_work_group_size: 1
    .uses_dynamic_stack: false
    .vgpr_count:     250
    .vgpr_spill_count: 0
    .wavefront_size: 64
  - .agpr_count:     0
    .args:
      - .actual_access:  read_only
        .address_space:  global
        .offset:         0
        .size:           8
        .value_kind:     global_buffer
      - .actual_access:  read_only
        .address_space:  global
        .offset:         8
        .size:           8
        .value_kind:     global_buffer
      - .actual_access:  read_only
        .address_space:  global
        .offset:         16
        .size:           8
        .value_kind:     global_buffer
      - .actual_access:  read_only
        .address_space:  global
        .offset:         24
        .size:           8
        .value_kind:     global_buffer
      - .actual_access:  read_only
        .address_space:  global
        .offset:         32
        .size:           8
        .value_kind:     global_buffer
      - .actual_access:  read_only
        .address_space:  global
        .offset:         40
        .size:           8
        .value_kind:     global_buffer
      - .address_space:  global
        .offset:         48
        .size:           8
        .value_kind:     global_buffer
    .group_segment_fixed_size: 2304
    .kernarg_segment_align: 8
    .kernarg_segment_size: 56
    .language:       OpenCL C
    .language_version:
      - 2
      - 0
    .max_flat_workgroup_size: 320
    .name:           _Z6k_agg1PKDF16_PK15HIP_vector_typeIiLj2EEPKtPKfS8_S8_Pf
    .private_segment_fixed_size: 0
    .sgpr_count:     40
    .sgpr_spill_count: 0
    .symbol:         _Z6k_agg1PKDF16_PK15HIP_vector_typeIiLj2EEPKtPKfS8_S8_Pf.kd
    .uniform_work_group_size: 1
    .uses_dynamic_stack: false
    .vgpr_count:     62
    .vgpr_spill_count: 0
    .wavefront_size: 64
  - .agpr_count:     0
    .args:
      - .actual_access:  read_only
        .address_space:  global
        .offset:         0
        .size:           8
        .value_kind:     global_buffer
      - .actual_access:  read_only
        .address_space:  global
        .offset:         8
        .size:           8
        .value_kind:     global_buffer
      - .actual_access:  read_only
        .address_space:  global
        .offset:         16
        .size:           8
        .value_kind:     global_buffer
      - .actual_access:  read_only
        .address_space:  global
        .offset:         24
        .size:           8
        .value_kind:     global_buffer
      - .actual_access:  read_only
        .address_space:  global
        .offset:         32
        .size:           8
        .value_kind:     global_buffer
      - .actual_access:  write_only
        .address_space:  global
        .offset:         40
        .size:           8
        .value_kind:     global_buffer
    .group_segment_fixed_size: 0
    .kernarg_segment_align: 8
    .kernarg_segment_size: 48
    .language:       OpenCL C
    .language_version:
      - 2
      - 0
    .max_flat_workgroup_size: 256
    .name:           _Z5k_outPKfPK15HIP_vector_typeIiLj2EEPKtS0_S0_Pf
    .private_segment_fixed_size: 0
    .sgpr_count:     18
    .sgpr_spill_count: 0
    .symbol:         _Z5k_outPKfPK15HIP_vector_typeIiLj2EEPKtS0_S0_Pf.kd
    .uniform_work_group_size: 1
    .uses_dynamic_stack: false
    .vgpr_count:     27
    .vgpr_spill_count: 0
    .wavefront_size: 64
